# first grid barrier: 16 arrival-counter loads issued back to back instead of 16 serial round trips
# speedup vs baseline: 1.0084x; 1.0084x over previous
; __device__ __forceinline__ unsigned xb_ld(unsigned* p)              { return __hip_atomic_load(p, __ATOMIC_RELAXED, __HIP_MEMORY_SCOPE_AGENT); }
; __device__ __forceinline__ void xcd_barrier_complete(unsigned* bar, unsigned x, unsigned& nloc, unsigned& nx) {
;     const unsigned G = gridDim.x * gridDim.y * gridDim.z;
;     unsigned sum, cnt, mine, sp = 0u;
;     for (;;) {
;         sum = 0u; cnt = 0u; mine = 0u;
; #pragma unroll
;         for (unsigned j = 0; j < 16; ++j) { const unsigned c = xb_ld(&bar[XB_XCNT(j)]); sum += c; cnt += (c > 0u) ? 1u : 0u; mine = (j == x) ? c : mine; }
;         if (sum == G) break;
;         __builtin_amdgcn_s_sleep(1);
;         if ((++sp & 255u) == 0u) { if (xb_ld(&bar[XB_TMO])) break; if (sp > XB_SPIN_CAP) { atomicAdd(&bar[XB_TMO], 1u); break; } }
;     }
;     nloc = mine > 0u ? mine : 1u; nx = cnt > 0u ? cnt : 1u;
; }
.LBB0_981:
	v_readlane_b32 s2, v254, 21
	v_readlane_b32 s3, v254, 22
	v_readlane_b32 s4, v254, 20
	s_mov_b64 s[20:21], -1
	s_nop 2
	global_load_dword v1, v3, s[2:3] sc1
	v_readlane_b32 s2, v254, 23
	v_readlane_b32 s3, v254, 24
	s_waitcnt lgkmcnt(0)
	s_nop 3
	global_load_dword v2, v3, s[2:3] sc1
	v_readlane_b32 s2, v254, 25
	v_readlane_b32 s3, v254, 26
	s_nop 4
	global_load_dword v4, v3, s[2:3] sc1
	v_readlane_b32 s2, v254, 27
	v_readlane_b32 s3, v254, 28
	s_nop 4
	global_load_dword v5, v3, s[2:3] sc1
	v_readlane_b32 s2, v254, 29
	v_readlane_b32 s3, v254, 30
	s_nop 4
	global_load_dword v6, v3, s[2:3] sc1
	v_readlane_b32 s2, v254, 31
	v_readlane_b32 s3, v254, 32
	s_nop 4
	global_load_dword v7, v3, s[2:3] sc1
	v_readlane_b32 s2, v254, 33
	v_readlane_b32 s3, v254, 34
	s_nop 4
	global_load_dword v8, v3, s[2:3] sc1
	v_readlane_b32 s2, v254, 35
	v_readlane_b32 s3, v254, 36
	s_nop 4
	global_load_dword v9, v3, s[2:3] sc1
	v_readlane_b32 s2, v254, 37
	v_readlane_b32 s3, v254, 38
	s_nop 4
	global_load_dword v10, v3, s[2:3] sc1
	v_readlane_b32 s2, v254, 39
	v_readlane_b32 s3, v254, 40
	s_nop 4
	global_load_dword v11, v3, s[2:3] sc1
	v_readlane_b32 s2, v254, 41
	v_readlane_b32 s3, v254, 42
	s_nop 4
	global_load_dword v12, v3, s[2:3] sc1
	v_readlane_b32 s2, v254, 43
	v_readlane_b32 s3, v254, 44
	s_nop 4
	global_load_dword v13, v3, s[2:3] sc1
	v_readlane_b32 s2, v254, 45
	v_readlane_b32 s3, v254, 46
	s_nop 4
	global_load_dword v14, v3, s[2:3] sc1
	v_readlane_b32 s2, v254, 47
	v_readlane_b32 s3, v254, 48
	s_nop 4
	global_load_dword v15, v3, s[2:3] sc1
	v_readlane_b32 s2, v254, 49
	v_readlane_b32 s3, v254, 50
	s_nop 4
	global_load_dword v16, v3, s[2:3] sc1
	v_readlane_b32 s2, v254, 51
	v_readlane_b32 s3, v254, 52
	s_nop 4
	global_load_dword v17, v3, s[2:3] sc1
	s_mov_b64 s[2:3], -1
	s_waitcnt vmcnt(0)
	v_add_u32_e32 v18, v2, v1
	v_add_u32_e32 v18, v18, v4
	v_add_u32_e32 v18, v18, v5
	v_add_u32_e32 v18, v18, v6
	v_add_u32_e32 v18, v18, v7
	v_add_u32_e32 v18, v18, v8
	v_add_u32_e32 v18, v18, v9
	v_add_u32_e32 v18, v18, v10
	v_add_u32_e32 v18, v18, v11
	v_add_u32_e32 v18, v18, v12
	v_add_u32_e32 v18, v18, v13
	v_add_u32_e32 v18, v18, v14
	v_add_u32_e32 v18, v18, v15
	v_add_u32_e32 v18, v18, v16
	v_add_u32_e32 v18, v18, v17
	v_cmp_eq_u32_e32 vcc, s4, v18
	s_cbranch_vccnz .LBB0_980
	s_and_b32 s2, s25, 0xff
	s_cmp_eq_u32 s2, 0
	s_mov_b64 s[2:3], -1
	s_mov_b64 s[28:29], -1
	s_sleep 1
	s_cbranch_scc0 .LBB0_985
	v_readlane_b32 s2, v253, 36
	v_readlane_b32 s3, v253, 37
	s_nop 4
	global_load_dword v18, v3, s[2:3] sc1
	s_waitcnt vmcnt(0)
	v_cmp_eq_u32_e32 vcc, 0, v18
	s_cbranch_vccnz .LBB0_987
	s_mov_b64 s[28:29], 0
	s_mov_b64 s[2:3], -1
